# speedup vs baseline: 1.0493x; 1.0065x over previous
.LBB2_4:
	ds_read_b128 v[114:117], v108 offset:16384
	ds_read_b128 v[118:121], v108 offset:17408
	ds_read_b128 v[122:125], v108 offset:18432
	ds_read_b128 v[126:129], v108 offset:19456
	s_add_i32 s43, s29, -1
	s_min_i32 s16, s43, s34
	s_min_i32 s14, s29, s34
	s_ashr_i32 s17, s16, 31
	s_ashr_i32 s15, s14, 31
	s_lshl_b64 s[16:17], s[16:17], 11
	s_mov_b32 m0, s35
	ds_read_b128 v[134:137], v109
	ds_read_b128 v[138:141], v109 offset:1024
	ds_read_b128 v[142:145], v109 offset:2048
	ds_read_b128 v[146:149], v109 offset:3072
	ds_read_b128 v[150:153], v109 offset:4096
	ds_read_b128 v[154:157], v109 offset:5120
	ds_read_b128 v[158:161], v109 offset:6144
	ds_read_b128 v[162:165], v109 offset:7168
	global_load_lds_dwordx4 v100, s[6:7]
	s_mov_b32 m0, s36
	s_nop 0
	global_load_lds_dwordx4 v102, s[6:7]
	s_waitcnt vmcnt(8)
	s_barrier
	s_waitcnt lgkmcnt(0)
	s_waitcnt lgkmcnt(0)
	v_mfma_f32_16x16x32_f16 v[94:97], v[114:117], v[134:137], v[94:97]
	v_mfma_f32_16x16x32_f16 v[90:93], v[122:125], v[134:137], v[90:93]
	v_mfma_f32_16x16x32_f16 v[86:89], v[114:117], v[142:145], v[86:89]
	v_mfma_f32_16x16x32_f16 v[82:85], v[122:125], v[142:145], v[82:85]
	v_mfma_f32_16x16x32_f16 v[78:81], v[114:117], v[150:153], v[78:81]
	v_mfma_f32_16x16x32_f16 v[74:77], v[122:125], v[150:153], v[74:77]
	v_mfma_f32_16x16x32_f16 v[70:73], v[114:117], v[158:161], v[70:73]
	v_mfma_f32_16x16x32_f16 v[66:69], v[122:125], v[158:161], v[66:69]
	v_mfma_f32_16x16x32_f16 v[94:97], v[118:121], v[138:141], v[94:97]
	v_mfma_f32_16x16x32_f16 v[90:93], v[126:129], v[138:141], v[90:93]
	v_mfma_f32_16x16x32_f16 v[86:89], v[118:121], v[146:149], v[86:89]
	v_mfma_f32_16x16x32_f16 v[82:85], v[126:129], v[146:149], v[82:85]
	v_mfma_f32_16x16x32_f16 v[78:81], v[118:121], v[154:157], v[78:81]
	v_mfma_f32_16x16x32_f16 v[74:77], v[126:129], v[154:157], v[74:77]
	v_mfma_f32_16x16x32_f16 v[70:73], v[118:121], v[162:165], v[70:73]
	v_mfma_f32_16x16x32_f16 v[66:69], v[126:129], v[162:165], v[66:69]
	s_barrier
	s_mov_b32 m0, s37
	ds_read_b128 v[114:117], v108 offset:32768
	ds_read_b128 v[118:121], v108 offset:33792
	ds_read_b128 v[122:125], v108 offset:34816
	ds_read_b128 v[126:129], v108 offset:35840
	global_load_lds_dwordx4 v104, s[6:7]
	s_mov_b32 m0, s38
	s_nop 0
	global_load_lds_dwordx4 v106, s[6:7]
	s_waitcnt vmcnt(8)
	s_barrier
	s_waitcnt lgkmcnt(0)
	s_waitcnt lgkmcnt(0)
	v_mfma_f32_16x16x32_f16 v[62:65], v[114:117], v[134:137], v[62:65]
	v_mfma_f32_16x16x32_f16 v[58:61], v[122:125], v[134:137], v[58:61]
	v_mfma_f32_16x16x32_f16 v[54:57], v[114:117], v[142:145], v[54:57]
	v_mfma_f32_16x16x32_f16 v[50:53], v[122:125], v[142:145], v[50:53]
	v_mfma_f32_16x16x32_f16 v[46:49], v[114:117], v[150:153], v[46:49]
	v_mfma_f32_16x16x32_f16 v[42:45], v[122:125], v[150:153], v[42:45]
	v_mfma_f32_16x16x32_f16 v[38:41], v[114:117], v[158:161], v[38:41]
	v_mfma_f32_16x16x32_f16 v[34:37], v[122:125], v[158:161], v[34:37]
	v_mfma_f32_16x16x32_f16 v[62:65], v[118:121], v[138:141], v[62:65]
	v_mfma_f32_16x16x32_f16 v[58:61], v[126:129], v[138:141], v[58:61]
	v_mfma_f32_16x16x32_f16 v[54:57], v[118:121], v[146:149], v[54:57]
	v_mfma_f32_16x16x32_f16 v[50:53], v[126:129], v[146:149], v[50:53]
	v_mfma_f32_16x16x32_f16 v[46:49], v[118:121], v[154:157], v[46:49]
	v_mfma_f32_16x16x32_f16 v[42:45], v[126:129], v[154:157], v[42:45]
	v_mfma_f32_16x16x32_f16 v[38:41], v[118:121], v[162:165], v[38:41]
	v_mfma_f32_16x16x32_f16 v[34:37], v[126:129], v[162:165], v[34:37]
	s_barrier
	s_add_u32 s44, s4, s16
	s_addc_u32 s45, s5, s17
	s_mov_b32 m0, s18
	ds_read_b128 v[114:117], v108 offset:49152
	ds_read_b128 v[118:121], v108 offset:50176
	ds_read_b128 v[122:125], v108 offset:51200
	ds_read_b128 v[126:129], v108 offset:52224
	global_load_lds_dwordx4 v130, s[44:45]
	s_add_u32 s46, s8, s16
	s_mov_b32 m0, s19
	s_addc_u32 s47, s9, s17
	global_load_lds_dwordx4 v98, s[44:45]
	s_mov_b32 m0, s20
	s_nop 0
	global_load_lds_dwordx4 v130, s[46:47]
	s_mov_b32 m0, s21
	s_nop 0
	global_load_lds_dwordx4 v98, s[46:47]
	s_waitcnt vmcnt(8)
	s_barrier
	s_waitcnt lgkmcnt(0)
	s_waitcnt lgkmcnt(0)
	v_mfma_f32_16x16x32_f16 v[30:33], v[114:117], v[134:137], v[30:33]
	v_mfma_f32_16x16x32_f16 v[26:29], v[122:125], v[134:137], v[26:29]
	v_mfma_f32_16x16x32_f16 v[22:25], v[114:117], v[142:145], v[22:25]
	v_mfma_f32_16x16x32_f16 v[18:21], v[122:125], v[142:145], v[18:21]
	v_mfma_f32_16x16x32_f16 v[14:17], v[114:117], v[150:153], v[14:17]
	v_mfma_f32_16x16x32_f16 v[10:13], v[122:125], v[150:153], v[10:13]
	v_mfma_f32_16x16x32_f16 v[6:9], v[114:117], v[158:161], v[6:9]
	v_mfma_f32_16x16x32_f16 v[2:5], v[122:125], v[158:161], v[2:5]
	v_mfma_f32_16x16x32_f16 v[30:33], v[118:121], v[138:141], v[30:33]
	v_mfma_f32_16x16x32_f16 v[26:29], v[126:129], v[138:141], v[26:29]
	v_mfma_f32_16x16x32_f16 v[22:25], v[118:121], v[146:149], v[22:25]
	v_mfma_f32_16x16x32_f16 v[18:21], v[126:129], v[146:149], v[18:21]
	v_mfma_f32_16x16x32_f16 v[14:17], v[118:121], v[154:157], v[14:17]
	v_mfma_f32_16x16x32_f16 v[10:13], v[126:129], v[154:157], v[10:13]
	v_mfma_f32_16x16x32_f16 v[6:9], v[118:121], v[162:165], v[6:9]
	v_mfma_f32_16x16x32_f16 v[2:5], v[126:129], v[162:165], v[2:5]
	s_barrier
	ds_read_b128 v[114:117], v110
	ds_read_b128 v[118:121], v110 offset:1024
	ds_read_b128 v[122:125], v110 offset:2048
	ds_read_b128 v[126:129], v110 offset:3072
	s_add_u32 s44, s10, s16
	s_addc_u32 s45, s11, s17
	s_mov_b32 m0, s22
	ds_read_b128 v[134:137], v111
	ds_read_b128 v[138:141], v111 offset:1024
	ds_read_b128 v[142:145], v111 offset:2048
	ds_read_b128 v[146:149], v111 offset:3072
	ds_read_b128 v[150:153], v111 offset:4096
	ds_read_b128 v[154:157], v111 offset:5120
	ds_read_b128 v[158:161], v111 offset:6144
	ds_read_b128 v[162:165], v111 offset:7168
	global_load_lds_dwordx4 v130, s[44:45]
	s_mov_b32 m0, s23
	s_nop 0
	global_load_lds_dwordx4 v98, s[44:45]
	s_waitcnt vmcnt(8)
	s_barrier
	s_waitcnt lgkmcnt(0)
	s_waitcnt lgkmcnt(0)
	v_mfma_f32_16x16x32_f16 v[94:97], v[114:117], v[134:137], v[94:97]
	v_mfma_f32_16x16x32_f16 v[90:93], v[122:125], v[134:137], v[90:93]
	v_mfma_f32_16x16x32_f16 v[86:89], v[114:117], v[142:145], v[86:89]
	v_mfma_f32_16x16x32_f16 v[82:85], v[122:125], v[142:145], v[82:85]
	v_mfma_f32_16x16x32_f16 v[78:81], v[114:117], v[150:153], v[78:81]
	v_mfma_f32_16x16x32_f16 v[74:77], v[122:125], v[150:153], v[74:77]
	v_mfma_f32_16x16x32_f16 v[70:73], v[114:117], v[158:161], v[70:73]
	v_mfma_f32_16x16x32_f16 v[66:69], v[122:125], v[158:161], v[66:69]
	v_mfma_f32_16x16x32_f16 v[94:97], v[118:121], v[138:141], v[94:97]
	v_mfma_f32_16x16x32_f16 v[90:93], v[126:129], v[138:141], v[90:93]
	v_mfma_f32_16x16x32_f16 v[86:89], v[118:121], v[146:149], v[86:89]
	v_mfma_f32_16x16x32_f16 v[82:85], v[126:129], v[146:149], v[82:85]
	v_mfma_f32_16x16x32_f16 v[78:81], v[118:121], v[154:157], v[78:81]
	v_mfma_f32_16x16x32_f16 v[74:77], v[126:129], v[154:157], v[74:77]
	v_mfma_f32_16x16x32_f16 v[70:73], v[118:121], v[162:165], v[70:73]
	v_mfma_f32_16x16x32_f16 v[66:69], v[126:129], v[162:165], v[66:69]
	s_barrier
	s_add_u32 s16, s12, s16
	s_addc_u32 s17, s13, s17
	s_mov_b32 m0, s26
	ds_read_b128 v[114:117], v112
	ds_read_b128 v[118:121], v112 offset:1024
	ds_read_b128 v[122:125], v112 offset:2048
	ds_read_b128 v[126:129], v112 offset:3072
	global_load_lds_dwordx4 v130, s[16:17]
	s_mov_b32 m0, s27
	s_nop 0
	global_load_lds_dwordx4 v98, s[16:17]
	s_waitcnt vmcnt(8)
	s_barrier
	s_waitcnt lgkmcnt(0)
	s_waitcnt lgkmcnt(0)
	v_mfma_f32_16x16x32_f16 v[62:65], v[114:117], v[134:137], v[62:65]
	v_mfma_f32_16x16x32_f16 v[58:61], v[122:125], v[134:137], v[58:61]
	v_mfma_f32_16x16x32_f16 v[54:57], v[114:117], v[142:145], v[54:57]
	v_mfma_f32_16x16x32_f16 v[50:53], v[122:125], v[142:145], v[50:53]
	v_mfma_f32_16x16x32_f16 v[46:49], v[114:117], v[150:153], v[46:49]
	v_mfma_f32_16x16x32_f16 v[42:45], v[122:125], v[150:153], v[42:45]
	v_mfma_f32_16x16x32_f16 v[38:41], v[114:117], v[158:161], v[38:41]
	v_mfma_f32_16x16x32_f16 v[34:37], v[122:125], v[158:161], v[34:37]
	v_mfma_f32_16x16x32_f16 v[62:65], v[118:121], v[138:141], v[62:65]
	v_mfma_f32_16x16x32_f16 v[58:61], v[126:129], v[138:141], v[58:61]
	v_mfma_f32_16x16x32_f16 v[54:57], v[118:121], v[146:149], v[54:57]
	v_mfma_f32_16x16x32_f16 v[50:53], v[126:129], v[146:149], v[50:53]
	v_mfma_f32_16x16x32_f16 v[46:49], v[118:121], v[154:157], v[46:49]
	v_mfma_f32_16x16x32_f16 v[42:45], v[126:129], v[154:157], v[42:45]
	v_mfma_f32_16x16x32_f16 v[38:41], v[118:121], v[162:165], v[38:41]
	v_mfma_f32_16x16x32_f16 v[34:37], v[126:129], v[162:165], v[34:37]
	s_barrier
	s_lshl_b64 s[14:15], s[14:15], 11
	s_add_u32 s16, s4, s14
	s_addc_u32 s17, s5, s15
	s_mov_b32 m0, s39
	s_add_u32 s14, s8, s14
	ds_read_b128 v[114:117], v113
	ds_read_b128 v[118:121], v113 offset:1024
	ds_read_b128 v[122:125], v113 offset:2048
	ds_read_b128 v[126:129], v113 offset:3072
	global_load_lds_dwordx4 v130, s[16:17]
	s_mov_b32 m0, s40
	s_addc_u32 s15, s9, s15
	global_load_lds_dwordx4 v98, s[16:17]
	s_mov_b32 m0, s41
	s_nop 0
	global_load_lds_dwordx4 v130, s[14:15]
	s_mov_b32 m0, s42
	s_nop 0
	global_load_lds_dwordx4 v98, s[14:15]
	s_waitcnt vmcnt(8)
	s_barrier
	s_waitcnt lgkmcnt(0)
	s_waitcnt lgkmcnt(0)
	v_mfma_f32_16x16x32_f16 v[30:33], v[114:117], v[134:137], v[30:33]
	v_mfma_f32_16x16x32_f16 v[26:29], v[122:125], v[134:137], v[26:29]
	v_mfma_f32_16x16x32_f16 v[22:25], v[114:117], v[142:145], v[22:25]
	v_mfma_f32_16x16x32_f16 v[18:21], v[122:125], v[142:145], v[18:21]
	v_mfma_f32_16x16x32_f16 v[14:17], v[114:117], v[150:153], v[14:17]
	v_mfma_f32_16x16x32_f16 v[10:13], v[122:125], v[150:153], v[10:13]
	v_mfma_f32_16x16x32_f16 v[6:9], v[114:117], v[158:161], v[6:9]
	v_mfma_f32_16x16x32_f16 v[2:5], v[122:125], v[158:161], v[2:5]
	v_mfma_f32_16x16x32_f16 v[30:33], v[118:121], v[138:141], v[30:33]
	v_mfma_f32_16x16x32_f16 v[26:29], v[126:129], v[138:141], v[26:29]
	v_mfma_f32_16x16x32_f16 v[22:25], v[118:121], v[146:149], v[22:25]
	v_mfma_f32_16x16x32_f16 v[18:21], v[126:129], v[146:149], v[18:21]
	v_mfma_f32_16x16x32_f16 v[14:17], v[118:121], v[154:157], v[14:17]
	v_mfma_f32_16x16x32_f16 v[10:13], v[126:129], v[154:157], v[10:13]
	v_mfma_f32_16x16x32_f16 v[6:9], v[118:121], v[162:165], v[6:9]
	v_mfma_f32_16x16x32_f16 v[2:5], v[126:129], v[162:165], v[2:5]
	s_barrier
	s_add_u32 s6, s6, 0x1000
	s_addc_u32 s7, s7, 0
	s_add_i32 s29, s29, 2
	s_cmp_ge_i32 s43, s33
	s_cbranch_scc0 .LBB2_4
	v_mov_b32_e32 v131, v97

.LBB3_4:
	v_add_u32_e32 v73, s16, v72
	ds_read_b128 v[74:77], v73 offset:16384
	ds_read_b128 v[78:81], v73 offset:17408
	ds_read_b128 v[82:85], v73 offset:18432
	ds_read_b128 v[86:89], v73 offset:19456
	s_add_i32 s18, s15, 2
	s_min_i32 s18, s18, s9
	s_ashr_i32 s19, s18, 31
	s_lshl_b64 s[18:19], s[18:19], 11
	s_add_u32 s20, s4, s18
	s_addc_u32 s21, s5, s19
	s_add_i32 s17, s14, s17
	v_add_u32_e32 v118, s16, v67
	s_mov_b32 m0, s17
	ds_read_b128 v[90:93], v118
	ds_read_b128 v[94:97], v118 offset:1024
	ds_read_b128 v[98:101], v118 offset:2048
	ds_read_b128 v[102:105], v118 offset:3072
	ds_read_b128 v[106:109], v118 offset:4096
	ds_read_b128 v[110:113], v118 offset:5120
	ds_read_b128 v[114:117], v118 offset:6144
	ds_read_b128 v[118:121], v118 offset:7168
	global_load_lds_dwordx4 v68, s[20:21]
	s_add_i32 m0, s17, 0x2000
	s_add_u32 s18, s6, s18
	s_addc_u32 s19, s7, s19
	global_load_lds_dwordx4 v70, s[20:21]
	s_add_i32 m0, s17, 0x4000
	s_nop 0
	global_load_lds_dwordx4 v68, s[18:19]
	s_add_i32 m0, s17, 0x6000
	s_nop 0
	global_load_lds_dwordx4 v70, s[18:19]
	s_waitcnt vmcnt(10)
	s_barrier
	s_waitcnt lgkmcnt(0)
	s_waitcnt lgkmcnt(0)
	v_mfma_f32_16x16x32_f16 v[62:65], v[74:77], v[90:93], v[62:65]
	v_mfma_f32_16x16x32_f16 v[46:49], v[82:85], v[90:93], v[46:49]
	v_mfma_f32_16x16x32_f16 v[58:61], v[74:77], v[98:101], v[58:61]
	v_mfma_f32_16x16x32_f16 v[42:45], v[82:85], v[98:101], v[42:45]
	v_mfma_f32_16x16x32_f16 v[54:57], v[74:77], v[106:109], v[54:57]
	v_mfma_f32_16x16x32_f16 v[38:41], v[82:85], v[106:109], v[38:41]
	v_mfma_f32_16x16x32_f16 v[50:53], v[74:77], v[114:117], v[50:53]
	v_mfma_f32_16x16x32_f16 v[26:29], v[82:85], v[114:117], v[26:29]
	v_mfma_f32_16x16x32_f16 v[62:65], v[78:81], v[94:97], v[62:65]
	v_mfma_f32_16x16x32_f16 v[46:49], v[86:89], v[94:97], v[46:49]
	v_mfma_f32_16x16x32_f16 v[58:61], v[78:81], v[102:105], v[58:61]
	v_mfma_f32_16x16x32_f16 v[42:45], v[86:89], v[102:105], v[42:45]
	v_mfma_f32_16x16x32_f16 v[54:57], v[78:81], v[110:113], v[54:57]
	v_mfma_f32_16x16x32_f16 v[38:41], v[86:89], v[110:113], v[38:41]
	v_mfma_f32_16x16x32_f16 v[50:53], v[78:81], v[118:121], v[50:53]
	v_mfma_f32_16x16x32_f16 v[26:29], v[86:89], v[118:121], v[26:29]
	s_barrier
	s_add_u32 s18, s18, s2
	s_addc_u32 s19, s19, s3
	s_add_i32 m0, s17, 0x8000
	ds_read_b128 v[74:77], v73 offset:32768
	ds_read_b128 v[78:81], v73 offset:33792
	ds_read_b128 v[82:85], v73 offset:34816
	ds_read_b128 v[86:89], v73 offset:35840
	global_load_lds_dwordx4 v68, s[18:19]
	s_add_i32 m0, s17, 0xa000
	s_nop 0
	global_load_lds_dwordx4 v70, s[18:19]
	s_waitcnt vmcnt(8)
	s_barrier
	s_waitcnt lgkmcnt(0)
	s_waitcnt lgkmcnt(0)
	v_mfma_f32_16x16x32_f16 v[34:37], v[74:77], v[90:93], v[34:37]
	v_mfma_f32_16x16x32_f16 v[14:17], v[82:85], v[90:93], v[14:17]
	v_mfma_f32_16x16x32_f16 v[30:33], v[74:77], v[98:101], v[30:33]
	v_mfma_f32_16x16x32_f16 v[10:13], v[82:85], v[98:101], v[10:13]
	v_mfma_f32_16x16x32_f16 v[22:25], v[74:77], v[106:109], v[22:25]
	v_mfma_f32_16x16x32_f16 v[6:9], v[82:85], v[106:109], v[6:9]
	v_mfma_f32_16x16x32_f16 v[18:21], v[74:77], v[114:117], v[18:21]
	v_mfma_f32_16x16x32_f16 v[2:5], v[82:85], v[114:117], v[2:5]
	v_mfma_f32_16x16x32_f16 v[34:37], v[78:81], v[94:97], v[34:37]
	v_mfma_f32_16x16x32_f16 v[14:17], v[86:89], v[94:97], v[14:17]
	v_mfma_f32_16x16x32_f16 v[30:33], v[78:81], v[102:105], v[30:33]
	v_mfma_f32_16x16x32_f16 v[10:13], v[86:89], v[102:105], v[10:13]
	v_mfma_f32_16x16x32_f16 v[22:25], v[78:81], v[110:113], v[22:25]
	v_mfma_f32_16x16x32_f16 v[6:9], v[86:89], v[110:113], v[6:9]
	v_mfma_f32_16x16x32_f16 v[18:21], v[78:81], v[118:121], v[18:21]
	v_mfma_f32_16x16x32_f16 v[2:5], v[86:89], v[118:121], v[2:5]
	s_barrier
	s_add_i32 s17, s16, 0xc000
	s_cmp_lg_u32 s17, 0x24000
	s_cselect_b32 s18, s17, 0
	s_add_i32 s15, s15, 1
	s_cmp_eq_u32 s8, s15
	s_mov_b32 s17, s16
	s_mov_b32 s16, s18
	s_cbranch_scc0 .LBB3_4
	v_mov_b32_e32 v69, v5
